# speedup vs baseline: 1.0263x; 1.0067x over previous
_Z6k_bcsrPK15HIP_vector_typeIiLj2EEPKiPiS5_:
	s_load_dwordx8 s[4:11], s[0:1], 0x0
	v_lshlrev_b32_e32 v1, 2, v0
	v_mov_b32_e32 v2, 0
	ds_write_b32 v1, v2
	ds_write_b32 v1, v2 offset:1024
	s_lshl_b32 s3, s2, 2
	s_waitcnt lgkmcnt(0)
	s_add_u32 s12, s6, s3
	s_addc_u32 s13, s7, 0
	s_load_dwordx2 s[14:15], s[12:13], 0x0
	s_lshl_b32 s16, s2, 9
	s_sub_u32 s17, s2, 0x30e
	s_lshl_b32 s17, s17, 6
	s_add_u32 s17, s17, 0x61a80
	s_cmpk_lt_u32 s2, 0x30e
	s_cselect_b32 s20, s16, s17
	s_mov_b32 s18, 0x668a0
	s_cselect_b32 s18, 0x61a80, s18
	s_cselect_b32 s19, 0x200, 64
	s_sub_u32 s22, s18, s20
	s_min_u32 s22, s22, s19
	s_waitcnt lgkmcnt(0)
	s_sub_u32 s21, s15, s14
	s_barrier
	s_mov_b32 s30, 0
	s_cmp_gt_u32 s21, 0x1000
	s_cbranch_scc1 .Lbc_slow1
	v_add_u32_e32 v3, s14, v0
	v_lshlrev_b32_e32 v3, 3, v3
	v_mov_b32_e32 v17, -1
	v_mov_b32_e32 v48, -1
	v_mov_b32_e32 v19, -1
	v_mov_b32_e32 v49, -1
	v_mov_b32_e32 v21, -1
	v_mov_b32_e32 v50, -1
	v_mov_b32_e32 v23, -1
	v_mov_b32_e32 v51, -1
	v_mov_b32_e32 v25, -1
	v_mov_b32_e32 v52, -1
	v_mov_b32_e32 v27, -1
	v_mov_b32_e32 v53, -1
	v_mov_b32_e32 v29, -1
	v_mov_b32_e32 v54, -1
	v_mov_b32_e32 v31, -1
	v_mov_b32_e32 v55, -1
	v_mov_b32_e32 v33, -1
	v_mov_b32_e32 v56, -1
	v_mov_b32_e32 v35, -1
	v_mov_b32_e32 v57, -1
	v_mov_b32_e32 v37, -1
	v_mov_b32_e32 v58, -1
	v_mov_b32_e32 v39, -1
	v_mov_b32_e32 v59, -1
	v_mov_b32_e32 v41, -1
	v_mov_b32_e32 v60, -1
	v_mov_b32_e32 v43, -1
	v_mov_b32_e32 v61, -1
	v_mov_b32_e32 v45, -1
	v_mov_b32_e32 v62, -1
	v_mov_b32_e32 v47, -1
	v_mov_b32_e32 v63, -1
	s_cmp_lt_u32 0, s21
	s_cbranch_scc0 .Lbc_ld_done
	v_add_u32_e32 v4, 0x0, v0
	v_cmp_gt_u32_e32 vcc, s21, v4
	s_and_saveexec_b64 s[32:33], vcc
	global_load_dwordx2 v[16:17], v3, s[4:5]
	s_mov_b64 exec, s[32:33]
	s_cmp_lt_u32 0x100, s21
	s_cbranch_scc0 .Lbc_ld_done
	v_add_u32_e32 v4, 0x100, v0
	v_cmp_gt_u32_e32 vcc, s21, v4
	s_and_saveexec_b64 s[32:33], vcc
	v_add_u32_e32 v5, 0x800, v3
	global_load_dwordx2 v[18:19], v5, s[4:5]
	s_mov_b64 exec, s[32:33]
	s_cmp_lt_u32 0x200, s21
	s_cbranch_scc0 .Lbc_ld_done
	v_add_u32_e32 v4, 0x200, v0
	v_cmp_gt_u32_e32 vcc, s21, v4
	s_and_saveexec_b64 s[32:33], vcc
	v_add_u32_e32 v5, 0x1000, v3
	global_load_dwordx2 v[20:21], v5, s[4:5]
	s_mov_b64 exec, s[32:33]
	s_cmp_lt_u32 0x300, s21
	s_cbranch_scc0 .Lbc_ld_done
	v_add_u32_e32 v4, 0x300, v0
	v_cmp_gt_u32_e32 vcc, s21, v4
	s_and_saveexec_b64 s[32:33], vcc
	v_add_u32_e32 v5, 0x1800, v3
	global_load_dwordx2 v[22:23], v5, s[4:5]
	s_mov_b64 exec, s[32:33]
	s_cmp_lt_u32 0x400, s21
	s_cbranch_scc0 .Lbc_ld_done
	v_add_u32_e32 v4, 0x400, v0
	v_cmp_gt_u32_e32 vcc, s21, v4
	s_and_saveexec_b64 s[32:33], vcc
	v_add_u32_e32 v5, 0x2000, v3
	global_load_dwordx2 v[24:25], v5, s[4:5]
	s_mov_b64 exec, s[32:33]
	s_cmp_lt_u32 0x500, s21
	s_cbranch_scc0 .Lbc_ld_done
	v_add_u32_e32 v4, 0x500, v0
	v_cmp_gt_u32_e32 vcc, s21, v4
	s_and_saveexec_b64 s[32:33], vcc
	v_add_u32_e32 v5, 0x2800, v3
	global_load_dwordx2 v[26:27], v5, s[4:5]
	s_mov_b64 exec, s[32:33]
	s_cmp_lt_u32 0x600, s21
	s_cbranch_scc0 .Lbc_ld_done
	v_add_u32_e32 v4, 0x600, v0
	v_cmp_gt_u32_e32 vcc, s21, v4
	s_and_saveexec_b64 s[32:33], vcc
	v_add_u32_e32 v5, 0x3000, v3
	global_load_dwordx2 v[28:29], v5, s[4:5]
	s_mov_b64 exec, s[32:33]
	s_cmp_lt_u32 0x700, s21
	s_cbranch_scc0 .Lbc_ld_done
	v_add_u32_e32 v4, 0x700, v0
	v_cmp_gt_u32_e32 vcc, s21, v4
	s_and_saveexec_b64 s[32:33], vcc
	v_add_u32_e32 v5, 0x3800, v3
	global_load_dwordx2 v[30:31], v5, s[4:5]
	s_mov_b64 exec, s[32:33]
	s_cmp_lt_u32 0x800, s21
	s_cbranch_scc0 .Lbc_ld_done
	v_add_u32_e32 v4, 0x800, v0
	v_cmp_gt_u32_e32 vcc, s21, v4
	s_and_saveexec_b64 s[32:33], vcc
	v_add_u32_e32 v5, 0x4000, v3
	global_load_dwordx2 v[32:33], v5, s[4:5]
	s_mov_b64 exec, s[32:33]
	s_cmp_lt_u32 0x900, s21
	s_cbranch_scc0 .Lbc_ld_done
	v_add_u32_e32 v4, 0x900, v0
	v_cmp_gt_u32_e32 vcc, s21, v4
	s_and_saveexec_b64 s[32:33], vcc
	v_add_u32_e32 v5, 0x4800, v3
	global_load_dwordx2 v[34:35], v5, s[4:5]
	s_mov_b64 exec, s[32:33]
	s_cmp_lt_u32 0xa00, s21
	s_cbranch_scc0 .Lbc_ld_done
	v_add_u32_e32 v4, 0xa00, v0
	v_cmp_gt_u32_e32 vcc, s21, v4
	s_and_saveexec_b64 s[32:33], vcc
	v_add_u32_e32 v5, 0x5000, v3
	global_load_dwordx2 v[36:37], v5, s[4:5]
	s_mov_b64 exec, s[32:33]
	s_cmp_lt_u32 0xb00, s21
	s_cbranch_scc0 .Lbc_ld_done
	v_add_u32_e32 v4, 0xb00, v0
	v_cmp_gt_u32_e32 vcc, s21, v4
	s_and_saveexec_b64 s[32:33], vcc
	v_add_u32_e32 v5, 0x5800, v3
	global_load_dwordx2 v[38:39], v5, s[4:5]
	s_mov_b64 exec, s[32:33]
	s_cmp_lt_u32 0xc00, s21
	s_cbranch_scc0 .Lbc_ld_done
	v_add_u32_e32 v4, 0xc00, v0
	v_cmp_gt_u32_e32 vcc, s21, v4
	s_and_saveexec_b64 s[32:33], vcc
	v_add_u32_e32 v5, 0x6000, v3
	global_load_dwordx2 v[40:41], v5, s[4:5]
	s_mov_b64 exec, s[32:33]
	s_cmp_lt_u32 0xd00, s21
	s_cbranch_scc0 .Lbc_ld_done
	v_add_u32_e32 v4, 0xd00, v0
	v_cmp_gt_u32_e32 vcc, s21, v4
	s_and_saveexec_b64 s[32:33], vcc
	v_add_u32_e32 v5, 0x6800, v3
	global_load_dwordx2 v[42:43], v5, s[4:5]
	s_mov_b64 exec, s[32:33]
	s_cmp_lt_u32 0xe00, s21
	s_cbranch_scc0 .Lbc_ld_done
	v_add_u32_e32 v4, 0xe00, v0
	v_cmp_gt_u32_e32 vcc, s21, v4
	s_and_saveexec_b64 s[32:33], vcc
	v_add_u32_e32 v5, 0x7000, v3
	global_load_dwordx2 v[44:45], v5, s[4:5]
	s_mov_b64 exec, s[32:33]
	s_cmp_lt_u32 0xf00, s21
	s_cbranch_scc0 .Lbc_ld_done
	v_add_u32_e32 v4, 0xf00, v0
	v_cmp_gt_u32_e32 vcc, s21, v4
	s_and_saveexec_b64 s[32:33], vcc
	v_add_u32_e32 v5, 0x7800, v3
	global_load_dwordx2 v[46:47], v5, s[4:5]
	s_mov_b64 exec, s[32:33]
.Lbc_ld_done:
	s_waitcnt vmcnt(0)
	v_mov_b32_e32 v6, 1
	s_cmp_lt_u32 0, s21
	s_cbranch_scc0 .Lbc_rk_done
	v_cmp_le_i32_e32 vcc, 0, v17
	s_and_saveexec_b64 s[32:33], vcc
	v_subrev_u32_e32 v17, s20, v17
	v_lshlrev_b32_e32 v7, 2, v17
	ds_add_rtn_u32 v48, v7, v6
	s_mov_b64 exec, s[32:33]
	s_cmp_lt_u32 0x100, s21
	s_cbranch_scc0 .Lbc_rk_done
	v_cmp_le_i32_e32 vcc, 0, v19
	s_and_saveexec_b64 s[32:33], vcc
	v_subrev_u32_e32 v19, s20, v19
	v_lshlrev_b32_e32 v7, 2, v19
	ds_add_rtn_u32 v49, v7, v6
	s_mov_b64 exec, s[32:33]
	s_cmp_lt_u32 0x200, s21
	s_cbranch_scc0 .Lbc_rk_done
	v_cmp_le_i32_e32 vcc, 0, v21
	s_and_saveexec_b64 s[32:33], vcc
	v_subrev_u32_e32 v21, s20, v21
	v_lshlrev_b32_e32 v7, 2, v21
	ds_add_rtn_u32 v50, v7, v6
	s_mov_b64 exec, s[32:33]
	s_cmp_lt_u32 0x300, s21
	s_cbranch_scc0 .Lbc_rk_done
	v_cmp_le_i32_e32 vcc, 0, v23
	s_and_saveexec_b64 s[32:33], vcc
	v_subrev_u32_e32 v23, s20, v23
	v_lshlrev_b32_e32 v7, 2, v23
	ds_add_rtn_u32 v51, v7, v6
	s_mov_b64 exec, s[32:33]
	s_cmp_lt_u32 0x400, s21
	s_cbranch_scc0 .Lbc_rk_done
	v_cmp_le_i32_e32 vcc, 0, v25
	s_and_saveexec_b64 s[32:33], vcc
	v_subrev_u32_e32 v25, s20, v25
	v_lshlrev_b32_e32 v7, 2, v25
	ds_add_rtn_u32 v52, v7, v6
	s_mov_b64 exec, s[32:33]
	s_cmp_lt_u32 0x500, s21
	s_cbranch_scc0 .Lbc_rk_done
	v_cmp_le_i32_e32 vcc, 0, v27
	s_and_saveexec_b64 s[32:33], vcc
	v_subrev_u32_e32 v27, s20, v27
	v_lshlrev_b32_e32 v7, 2, v27
	ds_add_rtn_u32 v53, v7, v6
	s_mov_b64 exec, s[32:33]
	s_cmp_lt_u32 0x600, s21
	s_cbranch_scc0 .Lbc_rk_done
	v_cmp_le_i32_e32 vcc, 0, v29
	s_and_saveexec_b64 s[32:33], vcc
	v_subrev_u32_e32 v29, s20, v29
	v_lshlrev_b32_e32 v7, 2, v29
	ds_add_rtn_u32 v54, v7, v6
	s_mov_b64 exec, s[32:33]
	s_cmp_lt_u32 0x700, s21
	s_cbranch_scc0 .Lbc_rk_done
	v_cmp_le_i32_e32 vcc, 0, v31
	s_and_saveexec_b64 s[32:33], vcc
	v_subrev_u32_e32 v31, s20, v31
	v_lshlrev_b32_e32 v7, 2, v31
	ds_add_rtn_u32 v55, v7, v6
	s_mov_b64 exec, s[32:33]
	s_cmp_lt_u32 0x800, s21
	s_cbranch_scc0 .Lbc_rk_done
	v_cmp_le_i32_e32 vcc, 0, v33
	s_and_saveexec_b64 s[32:33], vcc
	v_subrev_u32_e32 v33, s20, v33
	v_lshlrev_b32_e32 v7, 2, v33
	ds_add_rtn_u32 v56, v7, v6
	s_mov_b64 exec, s[32:33]
	s_cmp_lt_u32 0x900, s21
	s_cbranch_scc0 .Lbc_rk_done
	v_cmp_le_i32_e32 vcc, 0, v35
	s_and_saveexec_b64 s[32:33], vcc
	v_subrev_u32_e32 v35, s20, v35
	v_lshlrev_b32_e32 v7, 2, v35
	ds_add_rtn_u32 v57, v7, v6
	s_mov_b64 exec, s[32:33]
	s_cmp_lt_u32 0xa00, s21
	s_cbranch_scc0 .Lbc_rk_done
	v_cmp_le_i32_e32 vcc, 0, v37
	s_and_saveexec_b64 s[32:33], vcc
	v_subrev_u32_e32 v37, s20, v37
	v_lshlrev_b32_e32 v7, 2, v37
	ds_add_rtn_u32 v58, v7, v6
	s_mov_b64 exec, s[32:33]
	s_cmp_lt_u32 0xb00, s21
	s_cbranch_scc0 .Lbc_rk_done
	v_cmp_le_i32_e32 vcc, 0, v39
	s_and_saveexec_b64 s[32:33], vcc
	v_subrev_u32_e32 v39, s20, v39
	v_lshlrev_b32_e32 v7, 2, v39
	ds_add_rtn_u32 v59, v7, v6
	s_mov_b64 exec, s[32:33]
	s_cmp_lt_u32 0xc00, s21
	s_cbranch_scc0 .Lbc_rk_done
	v_cmp_le_i32_e32 vcc, 0, v41
	s_and_saveexec_b64 s[32:33], vcc
	v_subrev_u32_e32 v41, s20, v41
	v_lshlrev_b32_e32 v7, 2, v41
	ds_add_rtn_u32 v60, v7, v6
	s_mov_b64 exec, s[32:33]
	s_cmp_lt_u32 0xd00, s21
	s_cbranch_scc0 .Lbc_rk_done
	v_cmp_le_i32_e32 vcc, 0, v43
	s_and_saveexec_b64 s[32:33], vcc
	v_subrev_u32_e32 v43, s20, v43
	v_lshlrev_b32_e32 v7, 2, v43
	ds_add_rtn_u32 v61, v7, v6
	s_mov_b64 exec, s[32:33]
	s_cmp_lt_u32 0xe00, s21
	s_cbranch_scc0 .Lbc_rk_done
	v_cmp_le_i32_e32 vcc, 0, v45
	s_and_saveexec_b64 s[32:33], vcc
	v_subrev_u32_e32 v45, s20, v45
	v_lshlrev_b32_e32 v7, 2, v45
	ds_add_rtn_u32 v62, v7, v6
	s_mov_b64 exec, s[32:33]
	s_cmp_lt_u32 0xf00, s21
	s_cbranch_scc0 .Lbc_rk_done
	v_cmp_le_i32_e32 vcc, 0, v47
	s_and_saveexec_b64 s[32:33], vcc
	v_subrev_u32_e32 v47, s20, v47
	v_lshlrev_b32_e32 v7, 2, v47
	ds_add_rtn_u32 v63, v7, v6
	s_mov_b64 exec, s[32:33]
.Lbc_rk_done:
	s_waitcnt lgkmcnt(0)
	s_barrier
.Lbc_scan:
	v_lshlrev_b32_e32 v1, 3, v0
	ds_read_b64 v[8:9], v1
	s_waitcnt lgkmcnt(0)
	v_add_u32_e32 v10, v8, v9
	v_mov_b32_e32 v11, v10
	s_nop 1
	v_add_u32_dpp v11, v11, v11 row_shr:1 row_mask:0xf bank_mask:0xf bound_ctrl:0
	s_nop 1
	v_add_u32_dpp v11, v11, v11 row_shr:2 row_mask:0xf bank_mask:0xf bound_ctrl:0
	s_nop 1
	v_add_u32_dpp v11, v11, v11 row_shr:4 row_mask:0xf bank_mask:0xf bound_ctrl:0
	s_nop 1
	v_add_u32_dpp v11, v11, v11 row_shr:8 row_mask:0xf bank_mask:0xf bound_ctrl:0
	s_nop 1
	v_add_u32_dpp v11, v11, v11 row_bcast:15 row_mask:0xa bank_mask:0xf
	s_nop 1
	v_add_u32_dpp v11, v11, v11 row_bcast:31 row_mask:0xc bank_mask:0xf
	v_lshrrev_b32_e32 v12, 6, v0
	s_nop 0
	v_readfirstlane_b32 s3, v12
	v_readlane_b32 s16, v11, 63
	s_lshl_b32 s17, s3, 2
	s_add_u32 s17, s17, 0x1020
	v_mov_b32_e32 v12, s16
	v_mov_b32_e32 v13, s17
	s_mov_b64 s[32:33], exec
	s_mov_b64 exec, 1
	ds_write_b32 v13, v12
	s_mov_b64 exec, s[32:33]
	s_waitcnt lgkmcnt(0)
	s_barrier
	v_mov_b32_e32 v13, 0x1020
	ds_read_b128 v[12:15], v13
	v_mov_b32_e32 v2, 0
	s_waitcnt lgkmcnt(0)
	s_cmp_gt_u32 s3, 0
	s_cselect_b32 s16, 1, 0
	v_mad_u32_u24 v2, v12, s16, v2
	s_cmp_gt_u32 s3, 1
	s_cselect_b32 s16, 1, 0
	v_mad_u32_u24 v2, v13, s16, v2
	s_cmp_gt_u32 s3, 2
	s_cselect_b32 s16, 1, 0
	v_mad_u32_u24 v2, v14, s16, v2
	v_sub_u32_e32 v4, v11, v10
	v_add_u32_e32 v4, v4, v2
	v_add_u32_e32 v5, v4, v8
	ds_write_b64 v1, v[4:5] offset:2048
	v_add_u32_e32 v6, s14, v4
	v_add_u32_e32 v7, s14, v5
	v_lshlrev_b32_e32 v12, 1, v0
	v_add_lshl_u32 v13, v12, s20, 2
	v_cmp_gt_u32_e32 vcc, s22, v12
	s_and_saveexec_b64 s[32:33], vcc
	s_cbranch_execz .Lbc_nooff
	global_store_dwordx2 v13, v[6:7], s[8:9]
.Lbc_nooff:
	s_mov_b64 exec, s[32:33]
	s_cmpk_lg_u32 s2, 0x446
	s_cbranch_scc1 .Lbc_notlast
	v_cmp_eq_u32_e32 vcc, 0, v0
	s_and_saveexec_b64 s[32:33], vcc
	s_cbranch_execz .Lbc_notlast0
	v_mov_b32_e32 v12, 0x19a280
	v_mov_b32_e32 v13, s15
	global_store_dword v12, v13, s[8:9]
.Lbc_notlast0:
	s_mov_b64 exec, s[32:33]
.Lbc_notlast:
	s_waitcnt lgkmcnt(0)
	s_barrier
	s_cmp_lg_u32 s30, 0
	s_cbranch_scc1 .Lbc_slow2
	s_cmp_lt_u32 0, s21
	s_cbranch_scc0 .Lbc_rd_done
	v_max_i32_e32 v7, 0, v17
	v_lshlrev_b32_e32 v7, 2, v7
	ds_read_b32 v17, v7 offset:2048
	s_cmp_lt_u32 0x100, s21
	s_cbranch_scc0 .Lbc_rd_done
	v_max_i32_e32 v7, 0, v19
	v_lshlrev_b32_e32 v7, 2, v7
	ds_read_b32 v19, v7 offset:2048
	s_cmp_lt_u32 0x200, s21
	s_cbranch_scc0 .Lbc_rd_done
	v_max_i32_e32 v7, 0, v21
	v_lshlrev_b32_e32 v7, 2, v7
	ds_read_b32 v21, v7 offset:2048
	s_cmp_lt_u32 0x300, s21
	s_cbranch_scc0 .Lbc_rd_done
	v_max_i32_e32 v7, 0, v23
	v_lshlrev_b32_e32 v7, 2, v7
	ds_read_b32 v23, v7 offset:2048
	s_cmp_lt_u32 0x400, s21
	s_cbranch_scc0 .Lbc_rd_done
	v_max_i32_e32 v7, 0, v25
	v_lshlrev_b32_e32 v7, 2, v7
	ds_read_b32 v25, v7 offset:2048
	s_cmp_lt_u32 0x500, s21
	s_cbranch_scc0 .Lbc_rd_done
	v_max_i32_e32 v7, 0, v27
	v_lshlrev_b32_e32 v7, 2, v7
	ds_read_b32 v27, v7 offset:2048
	s_cmp_lt_u32 0x600, s21
	s_cbranch_scc0 .Lbc_rd_done
	v_max_i32_e32 v7, 0, v29
	v_lshlrev_b32_e32 v7, 2, v7
	ds_read_b32 v29, v7 offset:2048
	s_cmp_lt_u32 0x700, s21
	s_cbranch_scc0 .Lbc_rd_done
	v_max_i32_e32 v7, 0, v31
	v_lshlrev_b32_e32 v7, 2, v7
	ds_read_b32 v31, v7 offset:2048
	s_cmp_lt_u32 0x800, s21
	s_cbranch_scc0 .Lbc_rd_done
	v_max_i32_e32 v7, 0, v33
	v_lshlrev_b32_e32 v7, 2, v7
	ds_read_b32 v33, v7 offset:2048
	s_cmp_lt_u32 0x900, s21
	s_cbranch_scc0 .Lbc_rd_done
	v_max_i32_e32 v7, 0, v35
	v_lshlrev_b32_e32 v7, 2, v7
	ds_read_b32 v35, v7 offset:2048
	s_cmp_lt_u32 0xa00, s21
	s_cbranch_scc0 .Lbc_rd_done
	v_max_i32_e32 v7, 0, v37
	v_lshlrev_b32_e32 v7, 2, v7
	ds_read_b32 v37, v7 offset:2048
	s_cmp_lt_u32 0xb00, s21
	s_cbranch_scc0 .Lbc_rd_done
	v_max_i32_e32 v7, 0, v39
	v_lshlrev_b32_e32 v7, 2, v7
	ds_read_b32 v39, v7 offset:2048
	s_cmp_lt_u32 0xc00, s21
	s_cbranch_scc0 .Lbc_rd_done
	v_max_i32_e32 v7, 0, v41
	v_lshlrev_b32_e32 v7, 2, v7
	ds_read_b32 v41, v7 offset:2048
	s_cmp_lt_u32 0xd00, s21
	s_cbranch_scc0 .Lbc_rd_done
	v_max_i32_e32 v7, 0, v43
	v_lshlrev_b32_e32 v7, 2, v7
	ds_read_b32 v43, v7 offset:2048
	s_cmp_lt_u32 0xe00, s21
	s_cbranch_scc0 .Lbc_rd_done
	v_max_i32_e32 v7, 0, v45
	v_lshlrev_b32_e32 v7, 2, v7
	ds_read_b32 v45, v7 offset:2048
	s_cmp_lt_u32 0xf00, s21
	s_cbranch_scc0 .Lbc_rd_done
	v_max_i32_e32 v7, 0, v47
	v_lshlrev_b32_e32 v7, 2, v7
	ds_read_b32 v47, v7 offset:2048
.Lbc_rd_done:
	s_waitcnt lgkmcnt(0)
	s_cmp_lt_u32 0, s21
	s_cbranch_scc0 .Lbc_wr_done
	v_cmp_le_i32_e32 vcc, 0, v48
	s_and_saveexec_b64 s[32:33], vcc
	v_add_lshl_u32 v7, v17, v48, 2
	ds_write_b32 v7, v16 offset:4352
	s_mov_b64 exec, s[32:33]
	s_cmp_lt_u32 0x100, s21
	s_cbranch_scc0 .Lbc_wr_done
	v_cmp_le_i32_e32 vcc, 0, v49
	s_and_saveexec_b64 s[32:33], vcc
	v_add_lshl_u32 v7, v19, v49, 2
	ds_write_b32 v7, v18 offset:4352
	s_mov_b64 exec, s[32:33]
	s_cmp_lt_u32 0x200, s21
	s_cbranch_scc0 .Lbc_wr_done
	v_cmp_le_i32_e32 vcc, 0, v50
	s_and_saveexec_b64 s[32:33], vcc
	v_add_lshl_u32 v7, v21, v50, 2
	ds_write_b32 v7, v20 offset:4352
	s_mov_b64 exec, s[32:33]
	s_cmp_lt_u32 0x300, s21
	s_cbranch_scc0 .Lbc_wr_done
	v_cmp_le_i32_e32 vcc, 0, v51
	s_and_saveexec_b64 s[32:33], vcc
	v_add_lshl_u32 v7, v23, v51, 2
	ds_write_b32 v7, v22 offset:4352
	s_mov_b64 exec, s[32:33]
	s_cmp_lt_u32 0x400, s21
	s_cbranch_scc0 .Lbc_wr_done
	v_cmp_le_i32_e32 vcc, 0, v52
	s_and_saveexec_b64 s[32:33], vcc
	v_add_lshl_u32 v7, v25, v52, 2
	ds_write_b32 v7, v24 offset:4352
	s_mov_b64 exec, s[32:33]
	s_cmp_lt_u32 0x500, s21
	s_cbranch_scc0 .Lbc_wr_done
	v_cmp_le_i32_e32 vcc, 0, v53
	s_and_saveexec_b64 s[32:33], vcc
	v_add_lshl_u32 v7, v27, v53, 2
	ds_write_b32 v7, v26 offset:4352
	s_mov_b64 exec, s[32:33]
	s_cmp_lt_u32 0x600, s21
	s_cbranch_scc0 .Lbc_wr_done
	v_cmp_le_i32_e32 vcc, 0, v54
	s_and_saveexec_b64 s[32:33], vcc
	v_add_lshl_u32 v7, v29, v54, 2
	ds_write_b32 v7, v28 offset:4352
	s_mov_b64 exec, s[32:33]
	s_cmp_lt_u32 0x700, s21
	s_cbranch_scc0 .Lbc_wr_done
	v_cmp_le_i32_e32 vcc, 0, v55
	s_and_saveexec_b64 s[32:33], vcc
	v_add_lshl_u32 v7, v31, v55, 2
	ds_write_b32 v7, v30 offset:4352
	s_mov_b64 exec, s[32:33]
	s_cmp_lt_u32 0x800, s21
	s_cbranch_scc0 .Lbc_wr_done
	v_cmp_le_i32_e32 vcc, 0, v56
	s_and_saveexec_b64 s[32:33], vcc
	v_add_lshl_u32 v7, v33, v56, 2
	ds_write_b32 v7, v32 offset:4352
	s_mov_b64 exec, s[32:33]
	s_cmp_lt_u32 0x900, s21
	s_cbranch_scc0 .Lbc_wr_done
	v_cmp_le_i32_e32 vcc, 0, v57
	s_and_saveexec_b64 s[32:33], vcc
	v_add_lshl_u32 v7, v35, v57, 2
	ds_write_b32 v7, v34 offset:4352
	s_mov_b64 exec, s[32:33]
	s_cmp_lt_u32 0xa00, s21
	s_cbranch_scc0 .Lbc_wr_done
	v_cmp_le_i32_e32 vcc, 0, v58
	s_and_saveexec_b64 s[32:33], vcc
	v_add_lshl_u32 v7, v37, v58, 2
	ds_write_b32 v7, v36 offset:4352
	s_mov_b64 exec, s[32:33]
	s_cmp_lt_u32 0xb00, s21
	s_cbranch_scc0 .Lbc_wr_done
	v_cmp_le_i32_e32 vcc, 0, v59
	s_and_saveexec_b64 s[32:33], vcc
	v_add_lshl_u32 v7, v39, v59, 2
	ds_write_b32 v7, v38 offset:4352
	s_mov_b64 exec, s[32:33]
	s_cmp_lt_u32 0xc00, s21
	s_cbranch_scc0 .Lbc_wr_done
	v_cmp_le_i32_e32 vcc, 0, v60
	s_and_saveexec_b64 s[32:33], vcc
	v_add_lshl_u32 v7, v41, v60, 2
	ds_write_b32 v7, v40 offset:4352
	s_mov_b64 exec, s[32:33]
	s_cmp_lt_u32 0xd00, s21
	s_cbranch_scc0 .Lbc_wr_done
	v_cmp_le_i32_e32 vcc, 0, v61
	s_and_saveexec_b64 s[32:33], vcc
	v_add_lshl_u32 v7, v43, v61, 2
	ds_write_b32 v7, v42 offset:4352
	s_mov_b64 exec, s[32:33]
	s_cmp_lt_u32 0xe00, s21
	s_cbranch_scc0 .Lbc_wr_done
	v_cmp_le_i32_e32 vcc, 0, v62
	s_and_saveexec_b64 s[32:33], vcc
	v_add_lshl_u32 v7, v45, v62, 2
	ds_write_b32 v7, v44 offset:4352
	s_mov_b64 exec, s[32:33]
	s_cmp_lt_u32 0xf00, s21
	s_cbranch_scc0 .Lbc_wr_done
	v_cmp_le_i32_e32 vcc, 0, v63
	s_and_saveexec_b64 s[32:33], vcc
	v_add_lshl_u32 v7, v47, v63, 2
	ds_write_b32 v7, v46 offset:4352
	s_mov_b64 exec, s[32:33]
.Lbc_wr_done:
	s_waitcnt lgkmcnt(0)
	s_barrier
	s_sub_u32 s16, 0, s14
	s_and_b32 s16, s16, 3
	s_min_u32 s16, s16, s21
	s_sub_u32 s17, s21, s16
	s_lshr_b32 s18, s17, 2
	s_lshl_b32 s19, s18, 2
	s_add_u32 s19, s19, s16
	s_sub_u32 s23, s21, s19
	v_lshlrev_b32_e32 v1, 2, v0
	v_cmp_gt_u32_e32 vcc, s16, v0
	s_and_saveexec_b64 s[32:33], vcc
	s_cbranch_execz .Lbc_nohead
	ds_read_b32 v2, v1 offset:4352
	v_add_lshl_u32 v3, v0, s14, 2
	s_waitcnt lgkmcnt(0)
	global_store_dword v3, v2, s[10:11]
.Lbc_nohead:
	s_mov_b64 exec, s[32:33]
	v_mov_b32_e32 v2, v0
	v_cmp_gt_u32_e32 vcc, s18, v2
	s_and_saveexec_b64 s[32:33], vcc
	s_cbranch_execz .Lbc_nobody0
	v_lshl_add_u32 v3, v2, 2, s16
	v_lshlrev_b32_e32 v4, 2, v3
	v_add_u32_e32 v4, 0x1100, v4
	ds_read2_b32 v[8:9], v4 offset1:1
	ds_read2_b32 v[10:11], v4 offset0:2 offset1:3
	v_add_lshl_u32 v5, v3, s14, 2
	s_waitcnt lgkmcnt(0)
	global_store_dwordx4 v5, v[8:11], s[10:11] sc1
.Lbc_nobody0:
	s_mov_b64 exec, s[32:33]
	v_add_u32_e32 v2, 0x100, v0
	v_cmp_gt_u32_e32 vcc, s18, v2
	s_and_saveexec_b64 s[32:33], vcc
	s_cbranch_execz .Lbc_nobody1
	v_lshl_add_u32 v3, v2, 2, s16
	v_lshlrev_b32_e32 v4, 2, v3
	v_add_u32_e32 v4, 0x1100, v4
	ds_read2_b32 v[12:13], v4 offset1:1
	ds_read2_b32 v[14:15], v4 offset0:2 offset1:3
	v_add_lshl_u32 v5, v3, s14, 2
	s_waitcnt lgkmcnt(0)
	global_store_dwordx4 v5, v[12:15], s[10:11] sc1
.Lbc_nobody1:
	s_mov_b64 exec, s[32:33]
	v_add_u32_e32 v2, 0x200, v0
	v_cmp_gt_u32_e32 vcc, s18, v2
	s_and_saveexec_b64 s[32:33], vcc
	s_cbranch_execz .Lbc_nobody2
	v_lshl_add_u32 v3, v2, 2, s16
	v_lshlrev_b32_e32 v4, 2, v3
	v_add_u32_e32 v4, 0x1100, v4
	ds_read2_b32 v[16:17], v4 offset1:1
	ds_read2_b32 v[18:19], v4 offset0:2 offset1:3
	v_add_lshl_u32 v5, v3, s14, 2
	s_waitcnt lgkmcnt(0)
	global_store_dwordx4 v5, v[16:19], s[10:11] sc1
.Lbc_nobody2:
	s_mov_b64 exec, s[32:33]
	v_add_u32_e32 v2, 0x300, v0
	v_cmp_gt_u32_e32 vcc, s18, v2
	s_and_saveexec_b64 s[32:33], vcc
	s_cbranch_execz .Lbc_nobody3
	v_lshl_add_u32 v3, v2, 2, s16
	v_lshlrev_b32_e32 v4, 2, v3
	v_add_u32_e32 v4, 0x1100, v4
	ds_read2_b32 v[20:21], v4 offset1:1
	ds_read2_b32 v[22:23], v4 offset0:2 offset1:3
	v_add_lshl_u32 v5, v3, s14, 2
	s_waitcnt lgkmcnt(0)
	global_store_dwordx4 v5, v[20:23], s[10:11] sc1
.Lbc_nobody3:
	s_mov_b64 exec, s[32:33]
	v_cmp_gt_u32_e32 vcc, s23, v0
	s_and_saveexec_b64 s[32:33], vcc
	s_cbranch_execz .Lbc_notail
	v_add_u32_e32 v2, s19, v0
	v_lshlrev_b32_e32 v3, 2, v2
	ds_read_b32 v4, v3 offset:4352
	v_add_lshl_u32 v5, v2, s14, 2
	s_waitcnt lgkmcnt(0)
	global_store_dword v5, v4, s[10:11]
.Lbc_notail:
	s_mov_b64 exec, s[32:33]
	s_branch .Lbc_pl2
.Lbc_slow1:
	s_mov_b32 s30, 1
	v_mov_b32_e32 v2, v0
	v_mov_b32_e32 v6, 1
.Lbc_s1loop:
	v_cmp_gt_u32_e32 vcc, s21, v2
	s_and_b64 exec, exec, vcc
	s_cbranch_execz .Lbc_s1done
	v_add_lshl_u32 v3, v2, s14, 3
	global_load_dwordx2 v[16:17], v3, s[4:5]
	v_add_u32_e32 v2, 0x100, v2
	s_waitcnt vmcnt(0)
	v_subrev_u32_e32 v7, s20, v17
	v_lshlrev_b32_e32 v7, 2, v7
	ds_add_u32 v7, v6
	s_branch .Lbc_s1loop
.Lbc_s1done:
	s_mov_b64 exec, -1
	s_waitcnt lgkmcnt(0)
	s_barrier
	s_branch .Lbc_scan
.Lbc_slow2:
	v_lshlrev_b32_e32 v1, 2, v0
	v_mov_b32_e32 v2, 0
	ds_write_b32 v1, v2
	ds_write_b32 v1, v2 offset:1024
	s_waitcnt lgkmcnt(0)
	s_barrier
	v_mov_b32_e32 v2, v0
	v_mov_b32_e32 v6, 1
.Lbc_s2loop:
	v_cmp_gt_u32_e32 vcc, s21, v2
	s_and_b64 exec, exec, vcc
	s_cbranch_execz .Lbc_s2done
	v_add_lshl_u32 v3, v2, s14, 3
	global_load_dwordx2 v[16:17], v3, s[4:5]
	v_add_u32_e32 v2, 0x100, v2
	s_waitcnt vmcnt(0)
	v_subrev_u32_e32 v7, s20, v17
	v_lshlrev_b32_e32 v7, 2, v7
	ds_add_rtn_u32 v8, v7, v6
	ds_read_b32 v9, v7 offset:2048
	s_waitcnt lgkmcnt(0)
	v_add3_u32 v8, v8, v9, s14
	v_lshlrev_b32_e32 v8, 2, v8
	global_store_dword v8, v16, s[10:11]
	s_branch .Lbc_s2loop
.Lbc_s2done:
	s_mov_b64 exec, -1
.Lbc_pl:
	s_mov_b64 exec, -1
	s_waitcnt vmcnt(0) lgkmcnt(0)
	s_barrier
.Lbc_pl2:
	s_cmp_ge_u32 s20, 0x61a80
	s_cbranch_scc1 .Lpl_end
	v_lshlrev_b32_e32 v1, 3, v0
	ds_read_b64 v[4:5], v1 offset:2048
	ds_read_b32 v6, v1 offset:2056
	v_mov_b32_e32 v7, s21
	v_cmp_eq_u32_e32 vcc, 0xff, v0
	s_waitcnt lgkmcnt(0)
	s_nop 1
	v_cndmask_b32_e32 v6, v6, v7, vcc
	v_sub_u32_e32 v8, v5, v4
	v_sub_u32_e32 v9, v6, v5
	v_max_u32_e32 v10, v8, v9
	s_nop 1
	v_max_u32_dpp v10, v10, v10 quad_perm:[1,0,3,2] row_mask:0xf bank_mask:0xf
	s_nop 1
	v_max_u32_dpp v10, v10, v10 quad_perm:[2,3,0,1] row_mask:0xf bank_mask:0xf
	s_nop 1
	v_max_u32_dpp v10, v10, v10 row_half_mirror row_mask:0xf bank_mask:0xf
	v_lshrrev_b32_e32 v11, 3, v0
	s_lshr_b32 s0, s20, 4
	v_add_u32_e32 v11, s0, v11
	s_movk_i32 s1, 0x61a8
	v_cmp_gt_u32_e64 s[2:3], s1, v11
	s_add_u32 s24, s10, 0x712bd00
	s_addc_u32 s25, s11, 0
	s_add_u32 s16, s24, 0x186a000
	s_addc_u32 s17, s25, 0
	v_and_b32_e32 v12, 7, v0
	v_cmp_eq_u32_e32 vcc, 0, v12
	s_and_b64 s[18:19], vcc, s[2:3]
	v_lshlrev_b32_e32 v22, 2, v11
	s_and_saveexec_b64 s[12:13], s[18:19]
	s_cbranch_execz .Lpl_nom
	global_store_dword v22, v10, s[16:17]
.Lpl_nom:
	s_mov_b64 exec, s[12:13]
	v_min_u32_e32 v13, 16, v10
	v_lshlrev_b32_e32 v14, 10, v11
	v_lshlrev_b32_e32 v15, 1, v0
	v_and_b32_e32 v15, 15, v15
	v_lshl_add_u32 v14, v15, 2, v14
	v_mov_b32_e32 v20, 0
	v_mov_b32_e32 v21, 0x800000
	v_lshlrev_b32_e32 v16, 2, v4
	v_lshlrev_b32_e32 v17, 2, v5
	s_cmpk_lt_i32 s21, 0x1001
	s_cbranch_scc1 .Lpl_small
	v_add_u32_e32 v16, s14, v4
	v_add_u32_e32 v17, s14, v5
	v_lshlrev_b32_e32 v16, 2, v16
	v_lshlrev_b32_e32 v17, 2, v17

.Lpl_loop:
	v_cmp_lt_u32_e32 vcc, v20, v13
	s_and_b64 exec, exec, vcc
	s_cbranch_execz .Lpl_end
	s_cmpk_lt_i32 s21, 0x1001
	s_cbranch_scc0 .Lpl_big
	ds_read_b32 v18, v16 offset:4352
	ds_read_b32 v19, v17 offset:4352
	s_waitcnt lgkmcnt(0)
	s_branch .Lpl_sel

.Lpl_sel:
	v_cmp_lt_u32_e32 vcc, v20, v8
	v_add_u32_e32 v16, 4, v16
	v_add_u32_e32 v17, 4, v17
	v_cndmask_b32_e32 v18, v21, v18, vcc
	v_cmp_lt_u32_e32 vcc, v20, v9
	v_add_u32_e32 v20, 1, v20
	s_nop 0
	v_cndmask_b32_e32 v19, v21, v19, vcc
	global_store_dwordx2 v14, v[18:19], s[24:25]
	v_add_u32_e32 v14, 64, v14
	s_branch .Lpl_loop

	.amdhsa_kernel _Z6k_bcsrPK15HIP_vector_typeIiLj2EEPKiPiS5_
		.amdhsa_group_segment_fixed_size 20736
		.amdhsa_private_segment_fixed_size 0
		.amdhsa_kernarg_size 32
		.amdhsa_user_sgpr_count 2
		.amdhsa_user_sgpr_dispatch_ptr 0
		.amdhsa_user_sgpr_queue_ptr 0
		.amdhsa_user_sgpr_kernarg_segment_ptr 1
		.amdhsa_user_sgpr_dispatch_id 0
		.amdhsa_user_sgpr_kernarg_preload_length 0
		.amdhsa_user_sgpr_kernarg_preload_offset 0
		.amdhsa_user_sgpr_private_segment_size 0
		.amdhsa_uses_dynamic_stack 0
		.amdhsa_enable_private_segment 0
		.amdhsa_system_sgpr_workgroup_id_x 1
		.amdhsa_system_sgpr_workgroup_id_y 0
		.amdhsa_system_sgpr_workgroup_id_z 0
		.amdhsa_system_sgpr_workgroup_info 0
		.amdhsa_system_vgpr_workitem_id 0
		.amdhsa_next_free_vgpr 64
		.amdhsa_next_free_sgpr 34
		.amdhsa_accum_offset 64
		.amdhsa_reserve_vcc 1
		.amdhsa_float_round_mode_32 0
		.amdhsa_float_round_mode_16_64 0
		.amdhsa_float_denorm_mode_32 3
		.amdhsa_float_denorm_mode_16_64 3
		.amdhsa_dx10_clamp 1
		.amdhsa_ieee_mode 1
		.amdhsa_fp16_overflow 0
		.amdhsa_tg_split 0
		.amdhsa_exception_fp_ieee_invalid_op 0
		.amdhsa_exception_fp_denorm_src 0
		.amdhsa_exception_fp_ieee_div_zero 0
		.amdhsa_exception_fp_ieee_overflow 0
		.amdhsa_exception_fp_ieee_underflow 0
		.amdhsa_exception_fp_ieee_inexact 0
		.amdhsa_exception_int_div_zero 0
	.end_amdhsa_kernel

amdhsa.kernels:
  - .agpr_count:     0
    .args:
      - .actual_access:  read_only
        .address_space:  global
        .offset:         0
        .size:           8
        .value_kind:     global_buffer
      - .actual_access:  read_only
        .address_space:  global
        .offset:         8
        .size:           8
        .value_kind:     global_buffer
      - .actual_access:  write_only
        .address_space:  global
        .offset:         16
        .size:           8
        .value_kind:     global_buffer
      - .address_space:  global
        .offset:         24
        .size:           8
        .value_kind:     global_buffer
    .group_segment_fixed_size: 20736
    .kernarg_segment_align: 8
    .kernarg_segment_size: 32
    .language:       OpenCL C
    .language_version:
      - 2
      - 0
    .max_flat_workgroup_size: 256
    .name:           _Z6k_bcsrPK15HIP_vector_typeIiLj2EEPKiPiS5_
    .private_segment_fixed_size: 0
    .sgpr_count:     40
    .sgpr_spill_count: 0
    .symbol:         _Z6k_bcsrPK15HIP_vector_typeIiLj2EEPKiPiS5_.kd
    .uniform_work_group_size: 1
    .uses_dynamic_stack: false
    .vgpr_count:     64
    .vgpr_spill_count: 0
    .wavefront_size: 64
  - .agpr_count:     0
    .args:
      - .actual_access:  read_only
        .address_space:  global
        .offset:         0
        .size:           8
        .value_kind:     global_buffer
      - .actual_access:  read_only
        .address_space:  global
        .offset:         8
        .size:           8
        .value_kind:     global_buffer
      - .actual_access:  read_only
        .address_space:  global
        .offset:         16
        .size:           8
        .value_kind:     global_buffer
      - .actual_access:  write_only
        .address_space:  global
        .offset:         24
        .size:           8
        .value_kind:     global_buffer
      - .actual_access:  write_only
        .address_space:  global
        .offset:         32
        .size:           8
        .value_kind:     global_buffer
      - .actual_access:  read_only
        .address_space:  global
        .offset:         40
        .size:           8
        .value_kind:     global_buffer
      - .actual_access:  read_only
        .address_space:  global
        .offset:         48
        .size:           8
        .value_kind:     global_buffer
      - .actual_access:  read_only
        .address_space:  global
        .offset:         56
        .size:           8
        .value_kind:     global_buffer
      - .actual_access:  read_only
        .address_space:  global
        .offset:         64
        .size:           8
        .value_kind:     global_buffer
      - .actual_access:  read_only
        .address_space:  global
        .offset:         72
        .size:           8
        .value_kind:     global_buffer
      - .actual_access:  read_only
        .address_space:  global
        .offset:         80
        .size:           8
        .value_kind:     global_buffer
      - .actual_access:  read_only
        .address_space:  global
        .offset:         88
        .size:           8
        .value_kind:     global_buffer
      - .actual_access:  read_only
        .address_space:  global
        .offset:         96
        .size:           8
        .value_kind:     global_buffer
      - .address_space:  global
        .offset:         104
        .size:           8
        .value_kind:     global_buffer
      - .address_space:  global
        .offset:         112
        .size:           8
        .value_kind:     global_buffer
    .group_segment_fixed_size: 4384
    .kernarg_segment_align: 8
    .kernarg_segment_size: 120
    .language:       OpenCL C
    .language_version:
      - 2
      - 0
    .max_flat_workgroup_size: 1024
    .name:           _Z8k_bcountPKiS0_S0_PiPjPKfS4_S0_S0_S0_S4_S4_S4_PDF16_S5_
    .private_segment_fixed_size: 0
    .sgpr_count:     26
    .sgpr_spill_count: 0
    .symbol:         _Z8k_bcountPKiS0_S0_PiPjPKfS4_S0_S0_S0_S4_S4_S4_PDF16_S5_.kd
    .uniform_work_group_size: 1
    .uses_dynamic_stack: false
    .vgpr_count:     41
    .vgpr_spill_count: 0
    .wavefront_size: 64
  - .agpr_count:     0
    .args:
      - .actual_access:  read_only
        .address_space:  global
        .offset:         0
        .size:           8
        .value_kind:     global_buffer
      - .actual_access:  read_only
        .address_space:  global
        .offset:         8
        .size:           8
        .value_kind:     global_buffer
      - .actual_access:  read_only
        .address_space:  global
        .offset:         16
        .size:           8
        .value_kind:     global_buffer
      - .actual_access:  read_only
        .address_space:  global
        .offset:         24
        .size:           8
        .value_kind:     global_buffer
      - .actual_access:  write_only
        .address_space:  global
        .offset:         32
        .size:           8
        .value_kind:     global_buffer
      - .actual_access:  write_only
        .address_space:  global
        .offset:         40
        .size:           8
        .value_kind:     global_buffer
      - .actual_access:  read_only
        .address_space:  global
        .offset:         48
        .size:           8
        .value_kind:     global_buffer
      - .actual_access:  read_only
        .address_space:  global
        .offset:         56
        .size:           8
        .value_kind:     global_buffer
      - .actual_access:  read_only
        .address_space:  global
        .offset:         64
        .size:           8
        .value_kind:     global_buffer
      - .actual_access:  read_only
        .address_space:  global
        .offset:         72
        .size:           8
        .value_kind:     global_buffer
      - .actual_access:  read_only
        .address_space:  global
        .offset:         80
        .size:           8
        .value_kind:     global_buffer
      - .actual_access:  read_only
        .address_space:  global
        .offset:         88
        .size:           8
        .value_kind:     global_buffer
      - .actual_access:  read_only
        .address_space:  global
        .offset:         96
        .size:           8
        .value_kind:     global_buffer
      - .actual_access:  read_only
        .address_space:  global
        .offset:         104
        .size:           8
        .value_kind:     global_buffer
      - .address_space:  global
        .offset:         112
        .size:           8
        .value_kind:     global_buffer
      - .address_space:  global
        .offset:         120
        .size:           8
        .value_kind:     global_buffer
      - .offset:         128
        .size:           488
        .value_kind:     by_value
    .group_segment_fixed_size: 17024
    .kernarg_segment_align: 8
    .kernarg_segment_size: 616
    .language:       OpenCL C
    .language_version:
      - 2
      - 0
    .max_flat_workgroup_size: 1024
    .name:           _Z6k_prepPKiS0_S0_S0_PiP15HIP_vector_typeIiLj2EEPKfS6_S0_S0_S0_S6_S6_S6_PDF16_S7_6WSpecs
    .private_segment_fixed_size: 0
    .sgpr_count:     44
    .sgpr_spill_count: 0
    .symbol:         _Z6k_prepPKiS0_S0_S0_PiP15HIP_vector_typeIiLj2EEPKfS6_S0_S0_S0_S6_S6_S6_PDF16_S7_6WSpecs.kd
    .uniform_work_group_size: 1
    .uses_dynamic_stack: false
    .vgpr_count:     82
    .vgpr_spill_count: 0
    .wavefront_size: 64
  - .agpr_count:     0
    .args:
      - .offset:         0
        .size:           104
        .value_kind:     by_value
      - .offset:         104
        .size:           4
        .value_kind:     hidden_block_count_x
      - .offset:         108
        .size:           4
        .value_kind:     hidden_block_count_y
      - .offset:         112
        .size:           4
        .value_kind:     hidden_block_count_z
      - .offset:         116
        .size:           2
        .value_kind:     hidden_group_size_x
      - .offset:         118
        .size:           2
        .value_kind:     hidden_group_size_y
      - .offset:         120
        .size:           2
        .value_kind:     hidden_group_size_z
      - .offset:         122
        .size:           2
        .value_kind:     hidden_remainder_x
      - .offset:         124
        .size:           2
        .value_kind:     hidden_remainder_y
      - .offset:         126
        .size:           2
        .value_kind:     hidden_remainder_z
      - .offset:         144
        .size:           8
        .value_kind:     hidden_global_offset_x
      - .offset:         152
        .size:           8
        .value_kind:     hidden_global_offset_y
      - .offset:         160
        .size:           8
        .value_kind:     hidden_global_offset_z
      - .offset:         168
        .size:           2
        .value_kind:     hidden_grid_dims
    .group_segment_fixed_size: 155140
    .kernarg_segment_align: 8
    .kernarg_segment_size: 360
    .language:       OpenCL C
    .language_version:
      - 2
      - 0
    .max_flat_workgroup_size: 768
    .name:           _Z12k_layer_pool9LayerArgs
    .private_segment_fixed_size: 0
    .sgpr_count:     50
    .sgpr_spill_count: 0
    .symbol:         _Z12k_layer_pool9LayerArgs.kd
    .uniform_work_group_size: 1
    .uses_dynamic_stack: false
    .vgpr_count:     168
    .vgpr_spill_count: 0
    .wavefront_size: 64
  - .agpr_count:     0
    .args:
      - .actual_access:  read_only
        .address_space:  global
        .offset:         0
        .size:           8
        .value_kind:     global_buffer
      - .actual_access:  read_only
        .address_space:  global
        .offset:         8
        .size:           8
        .value_kind:     global_buffer
      - .actual_access:  read_only
        .address_space:  global
        .offset:         16
        .size:           8
        .value_kind:     global_buffer
      - .actual_access:  read_only
        .address_space:  global
        .offset:         24
        .size:           8
        .value_kind:     global_buffer
      - .actual_access:  read_only
        .address_space:  global
        .offset:         32
        .size:           8
        .value_kind:     global_buffer
      - .actual_access:  read_only
        .address_space:  global
        .offset:         40
        .size:           8
        .value_kind:     global_buffer
      - .actual_access:  read_only
        .address_space:  global
        .offset:         48
        .size:           8
        .value_kind:     global_buffer
      - .actual_access:  write_only
        .address_space:  global
        .offset:         56
        .size:           8
        .value_kind:     global_buffer
    .group_segment_fixed_size: 2560
    .kernarg_segment_align: 8
    .kernarg_segment_size: 64
    .language:       OpenCL C
    .language_version:
      - 2
      - 0
    .max_flat_workgroup_size: 512
    .name:           _Z5k_mlpPKjPKfS2_S2_S2_S2_S2_Pf
    .private_segment_fixed_size: 0
    .sgpr_count:     18
    .sgpr_spill_count: 0
    .symbol:         _Z5k_mlpPKjPKfS2_S2_S2_S2_S2_Pf.kd
    .uniform_work_group_size: 1
    .uses_dynamic_stack: false
    .vgpr_count:     120
    .vgpr_spill_count: 0
    .wavefront_size: 64
  - .agpr_count:     0
    .args:
      - .offset:         0
        .size:           104
        .value_kind:     by_value
      - .offset:         104
        .size:           104
        .value_kind:     by_value
      - .offset:         208
        .size:           4
        .value_kind:     by_value
      - .offset:         216
        .size:           4
        .value_kind:     hidden_block_count_x
      - .offset:         220
        .size:           4
        .value_kind:     hidden_block_count_y
      - .offset:         224
        .size:           4
        .value_kind:     hidden_block_count_z
      - .offset:         228
        .size:           2
        .value_kind:     hidden_group_size_x
      - .offset:         230
        .size:           2
        .value_kind:     hidden_group_size_y
      - .offset:         232
        .size:           2
        .value_kind:     hidden_group_size_z
      - .offset:         234
        .size:           2
        .value_kind:     hidden_remainder_x
      - .offset:         236
        .size:           2
        .value_kind:     hidden_remainder_y
      - .offset:         238
        .size:           2
        .value_kind:     hidden_remainder_z
      - .offset:         256
        .size:           8
        .value_kind:     hidden_global_offset_x
      - .offset:         264
        .size:           8
        .value_kind:     hidden_global_offset_y
      - .offset:         272
        .size:           8
        .value_kind:     hidden_global_offset_z
      - .offset:         280
        .size:           2
        .value_kind:     hidden_grid_dims
    .group_segment_fixed_size: 151044
    .kernarg_segment_align: 8
    .kernarg_segment_size: 472
    .language:       OpenCL C
    .language_version:
      - 2
      - 0
    .max_flat_workgroup_size: 768
    .name:           _Z10k_layer_fhILi96ELb1EEv9LayerArgsS0_i
    .private_segment_fixed_size: 0
    .sgpr_count:     52
    .sgpr_spill_count: 0
    .symbol:         _Z10k_layer_fhILi96ELb1EEv9LayerArgsS0_i.kd
    .uniform_work_group_size: 1
    .uses_dynamic_stack: false
    .vgpr_count:     168
    .vgpr_spill_count: 0
    .wavefront_size: 64
  - .agpr_count:     0
    .args:
      - .offset:         0
        .size:           104
        .value_kind:     by_value
      - .offset:         104
        .size:           104
        .value_kind:     by_value
      - .offset:         208
        .size:           4
        .value_kind:     by_value
      - .offset:         216
        .size:           4
        .value_kind:     hidden_block_count_x
      - .offset:         220
        .size:           4
        .value_kind:     hidden_block_count_y
      - .offset:         224
        .size:           4
        .value_kind:     hidden_block_count_z
      - .offset:         228
        .size:           2
        .value_kind:     hidden_group_size_x
      - .offset:         230
        .size:           2
        .value_kind:     hidden_group_size_y
      - .offset:         232
        .size:           2
        .value_kind:     hidden_group_size_z
      - .offset:         234
        .size:           2
        .value_kind:     hidden_remainder_x
      - .offset:         236
        .size:           2
        .value_kind:     hidden_remainder_y
      - .offset:         238
        .size:           2
        .value_kind:     hidden_remainder_z
      - .offset:         256
        .size:           8
        .value_kind:     hidden_global_offset_x
      - .offset:         264
        .size:           8
        .value_kind:     hidden_global_offset_y
      - .offset:         272
        .size:           8
        .value_kind:     hidden_global_offset_z
      - .offset:         280
        .size:           2
        .value_kind:     hidden_grid_dims
    .group_segment_fixed_size: 151044
    .kernarg_segment_align: 8
    .kernarg_segment_size: 472
    .language:       OpenCL C
    .language_version:
      - 2
      - 0
    .max_flat_workgroup_size: 768
    .name:           _Z10k_layer_fhILi128ELb1EEv9LayerArgsS0_i
    .private_segment_fixed_size: 0
    .sgpr_count:     45
    .sgpr_spill_count: 0
    .symbol:         _Z10k_layer_fhILi128ELb1EEv9LayerArgsS0_i.kd
    .uniform_work_group_size: 1
    .uses_dynamic_stack: false
    .vgpr_count:     168
    .vgpr_spill_count: 0
    .wavefront_size: 64
